# same, fallback copy placed after the kernel end (code placement)
# speedup vs baseline: 1.0049x; 1.0049x over previous
.LBB0_1541:
	s_endpgm
.Lgqa_slow_873:
	v_exp_f32_e32 v101, v80
	v_exp_f32_e32 v103, v81
	v_exp_f32_e32 v111, v88
	v_exp_f32_e32 v89, v89
	v_exp_f32_e32 v105, v82
	v_exp_f32_e32 v113, v90
	v_exp_f32_e32 v83, v83
	v_exp_f32_e32 v91, v91
	v_exp_f32_e32 v107, v84
	v_exp_f32_e32 v115, v92
	v_mov_b32_e32 v100, v64
	v_mov_b32_e32 v102, v65
	v_mov_b32_e32 v110, v72
	v_mov_b32_e32 v88, v73
	v_exp_f32_e32 v85, v85
	v_exp_f32_e32 v93, v93
	v_pk_add_f32 v[80:81], v[100:101], v[102:103]
	v_pk_add_f32 v[118:119], v[110:111], v[88:89]
	v_mov_b32_e32 v104, v66
	v_mov_b32_e32 v112, v74
	v_exp_f32_e32 v109, v86
	v_exp_f32_e32 v117, v94
	v_pk_add_f32 v[80:81], v[104:105], v[80:81]
	v_pk_add_f32 v[118:119], v[112:113], v[118:119]
	v_mov_b32_e32 v82, v67
	v_mov_b32_e32 v90, v75
	v_exp_f32_e32 v87, v87
	v_exp_f32_e32 v95, v95
	v_pk_add_f32 v[80:81], v[82:83], v[80:81]
	v_pk_add_f32 v[118:119], v[90:91], v[118:119]
	v_mov_b32_e32 v106, v68
	v_mov_b32_e32 v114, v76
	v_pk_add_f32 v[80:81], v[106:107], v[80:81]
	v_pk_add_f32 v[118:119], v[114:115], v[118:119]
	v_mov_b32_e32 v84, v69
	v_mov_b32_e32 v92, v77
	v_pk_add_f32 v[80:81], v[84:85], v[80:81]
	v_pk_add_f32 v[118:119], v[92:93], v[118:119]
	v_mov_b32_e32 v108, v70
	v_mov_b32_e32 v116, v78
	v_pk_add_f32 v[80:81], v[108:109], v[80:81]
	v_pk_add_f32 v[118:119], v[116:117], v[118:119]
	v_mov_b32_e32 v86, v71
	v_mov_b32_e32 v94, v79
	v_pk_add_f32 v[80:81], v[86:87], v[80:81]
	v_pk_add_f32 v[118:119], v[94:95], v[118:119]
	s_lshl_b32 s2, s33, 12
	v_pk_add_f32 v[80:81], v[118:119], v[80:81]
	s_add_u32 s8, s35, s2
	v_pk_add_f32 v[80:81], v[80:81], v[80:81] op_sel:[0,1] op_sel_hi:[1,0]
	s_addc_u32 s9, s36, 0
	s_lshl_b32 s2, s28, 7
	v_mov_b32_e32 v99, v80
	s_ashr_i32 s3, s2, 31
	s_nop 0
	v_permlane32_swap_b32_e32 v80, v99
	s_lshl_b64 s[2:3], s[2:3], 1
	v_mul_f32_e32 v96, v217, v208
	v_add_f32_e32 v98, v142, v143
	v_mov_b32_e32 v97, v80
	s_add_u32 s8, s8, s2
	v_pk_add_f32 v[80:81], v[96:97], v[98:99]
	v_cvt_pk_bf16_f32 v64, v64, v65
	v_cvt_pk_bf16_f32 v65, v66, v67
	v_cvt_pk_bf16_f32 v66, v68, v69
	v_cvt_pk_bf16_f32 v67, v70, v71
	v_cvt_pk_bf16_f32 v68, v72, v73
	v_cvt_pk_bf16_f32 v69, v74, v75
	v_cvt_pk_bf16_f32 v70, v76, v77
	v_cvt_pk_bf16_f32 v71, v78, v79
	v_cvt_pk_bf16_f32 v72, v101, v103
	v_cvt_pk_bf16_f32 v73, v105, v83
	v_cvt_pk_bf16_f32 v74, v107, v85
	v_cvt_pk_bf16_f32 v75, v109, v87
	v_cvt_pk_bf16_f32 v76, v111, v89
	v_cvt_pk_bf16_f32 v77, v113, v91
	v_cvt_pk_bf16_f32 v78, v115, v93
	v_cvt_pk_bf16_f32 v79, v117, v95
	s_addc_u32 s9, s9, s3
	v_fmac_f32_e32 v81, v80, v128
	v_permlane32_swap_b32_e32 v64, v66
	v_permlane32_swap_b32_e32 v65, v67
	v_permlane32_swap_b32_e32 v68, v70
	v_permlane32_swap_b32_e32 v69, v71
	v_permlane32_swap_b32_e32 v72, v74
	v_permlane32_swap_b32_e32 v73, v75
	v_permlane32_swap_b32_e32 v76, v78
	v_permlane32_swap_b32_e32 v77, v79
	ds_read_b64_tr_b16 v[82:83], v211 offset:0
	ds_read_b64_tr_b16 v[84:85], v211 offset:0x800
	ds_read_b64_tr_b16 v[86:87], v211 offset:0x1000
	ds_read_b64_tr_b16 v[88:89], v211 offset:0x1800
	ds_read_b64_tr_b16 v[90:91], v211 offset:0x2000
	ds_read_b64_tr_b16 v[92:93], v211 offset:0x2800
	ds_read_b64_tr_b16 v[94:95], v211 offset:0x3000
	ds_read_b64_tr_b16 v[96:97], v211 offset:0x3800
	s_waitcnt lgkmcnt(0)
	s_nop 0
	v_mfma_f32_32x32x16_bf16 v[0:15], v[82:85], v[64:67], v[0:15]
	ds_read_b64_tr_b16 v[82:83], v211 offset:0x200
	ds_read_b64_tr_b16 v[84:85], v211 offset:0xa00
	v_mfma_f32_32x32x16_bf16 v[0:15], v[86:89], v[68:71], v[0:15]
	ds_read_b64_tr_b16 v[86:87], v211 offset:0x1200
	ds_read_b64_tr_b16 v[88:89], v211 offset:0x1a00
	v_mfma_f32_32x32x16_bf16 v[0:15], v[90:93], v[72:75], v[0:15]
	ds_read_b64_tr_b16 v[90:91], v211 offset:0x2200
	ds_read_b64_tr_b16 v[92:93], v211 offset:0x2a00
	v_mfma_f32_32x32x16_bf16 v[0:15], v[94:97], v[76:79], v[0:15]
	ds_read_b64_tr_b16 v[94:95], v211 offset:0x3200
	ds_read_b64_tr_b16 v[96:97], v211 offset:0x3a00
	s_waitcnt lgkmcnt(0)
	v_mfma_f32_32x32x16_bf16 v[48:63], v[82:85], v[64:67], v[48:63]
	ds_read_b64_tr_b16 v[82:83], v211 offset:0x400
	ds_read_b64_tr_b16 v[84:85], v211 offset:0xc00
	v_mfma_f32_32x32x16_bf16 v[48:63], v[86:89], v[68:71], v[48:63]
	ds_read_b64_tr_b16 v[86:87], v211 offset:0x1400
	ds_read_b64_tr_b16 v[88:89], v211 offset:0x1c00
	v_mfma_f32_32x32x16_bf16 v[48:63], v[90:93], v[72:75], v[48:63]
	ds_read_b64_tr_b16 v[90:91], v211 offset:0x2400
	ds_read_b64_tr_b16 v[92:93], v211 offset:0x2c00
	v_mfma_f32_32x32x16_bf16 v[48:63], v[94:97], v[76:79], v[48:63]
	ds_read_b64_tr_b16 v[94:95], v211 offset:0x3400
	ds_read_b64_tr_b16 v[96:97], v211 offset:0x3c00
	s_waitcnt lgkmcnt(0)
	v_mfma_f32_32x32x16_bf16 v[32:47], v[82:85], v[64:67], v[32:47]
	ds_read_b64_tr_b16 v[82:83], v211 offset:0x600
	ds_read_b64_tr_b16 v[84:85], v211 offset:0xe00
	v_mfma_f32_32x32x16_bf16 v[32:47], v[86:89], v[68:71], v[32:47]
	ds_read_b64_tr_b16 v[86:87], v211 offset:0x1600
	ds_read_b64_tr_b16 v[88:89], v211 offset:0x1e00
	v_mfma_f32_32x32x16_bf16 v[32:47], v[90:93], v[72:75], v[32:47]
	ds_read_b64_tr_b16 v[90:91], v211 offset:0x2600
	ds_read_b64_tr_b16 v[92:93], v211 offset:0x2e00
	v_mfma_f32_32x32x16_bf16 v[32:47], v[94:97], v[76:79], v[32:47]
	ds_read_b64_tr_b16 v[94:95], v211 offset:0x3600
	ds_read_b64_tr_b16 v[96:97], v211 offset:0x3e00
	s_waitcnt lgkmcnt(0)
	v_mfma_f32_32x32x16_bf16 v[16:31], v[82:85], v[64:67], v[16:31]
	v_rcp_f32_e32 v67, v81
	v_mbcnt_lo_u32_b32 v66, -1, 0
	v_mbcnt_hi_u32_b32 v66, -1, v66
	s_add_i32 s20, s20, 1
	v_add_u32_e32 v64, s80, v66
	v_ashrrev_i32_e32 v64, 1, v64
	v_mul_f32_e32 v0, v67, v0
	v_mul_f32_e32 v1, v67, v1
	v_bfi_b32 v64, s84, v64, v66
	v_cvt_pk_bf16_f32 v0, v0, v1
	v_mul_f32_e32 v1, v67, v2
	v_mul_f32_e32 v2, v67, v3
	v_ashrrev_i32_e32 v65, 31, v64
	v_cvt_pk_bf16_f32 v1, v1, v2
	v_mul_f32_e32 v2, v67, v4
	v_mul_f32_e32 v3, v67, v5
	v_lshlrev_b64 v[64:65], 12, v[64:65]
	v_lshrrev_b32_e32 v66, 1, v66
	v_cvt_pk_bf16_f32 v2, v2, v3
	v_mul_f32_e32 v3, v67, v6
	v_lshl_add_u64 v[64:65], s[8:9], 0, v[64:65]
	v_and_b32_e32 v128, 16, v66
	v_mul_f32_e32 v4, v67, v7
	v_cvt_pk_bf16_f32 v3, v3, v4
	v_lshl_add_u64 v[64:65], v[64:65], 0, v[128:129]
	v_permlane32_swap_b32_e32 v0, v2
	v_permlane32_swap_b32_e32 v1, v3
	global_store_dwordx4 v[64:65], v[0:3], off
	v_mul_f32_e32 v4, v67, v15
	v_mfma_f32_32x32x16_bf16 v[16:31], v[86:89], v[68:71], v[16:31]
	v_mul_f32_e32 v0, v67, v8
	v_mul_f32_e32 v1, v67, v9
	v_cvt_pk_bf16_f32 v0, v0, v1
	v_mul_f32_e32 v1, v67, v10
	v_mul_f32_e32 v2, v67, v11
	v_cvt_pk_bf16_f32 v1, v1, v2
	v_mul_f32_e32 v2, v67, v12
	v_mul_f32_e32 v3, v67, v13
	v_cvt_pk_bf16_f32 v2, v2, v3
	v_mul_f32_e32 v3, v67, v14
	v_cvt_pk_bf16_f32 v3, v3, v4
	v_permlane32_swap_b32_e32 v0, v2
	s_nop 0
	v_permlane32_swap_b32_e32 v1, v3
	global_store_dwordx4 v[64:65], v[0:3], off offset:32
	v_mul_f32_e32 v4, v67, v55
	v_mfma_f32_32x32x16_bf16 v[16:31], v[90:93], v[72:75], v[16:31]
	v_mul_f32_e32 v0, v67, v48
	v_mul_f32_e32 v1, v67, v49
	v_cvt_pk_bf16_f32 v0, v0, v1
	v_mul_f32_e32 v1, v67, v50
	v_mul_f32_e32 v2, v67, v51
	v_cvt_pk_bf16_f32 v1, v1, v2
	v_mul_f32_e32 v2, v67, v52
	v_mul_f32_e32 v3, v67, v53
	v_cvt_pk_bf16_f32 v2, v2, v3
	v_mul_f32_e32 v3, v67, v54
	v_cvt_pk_bf16_f32 v3, v3, v4
	v_permlane32_swap_b32_e32 v0, v2
	s_nop 0
	v_permlane32_swap_b32_e32 v1, v3
	global_store_dwordx4 v[64:65], v[0:3], off offset:64
	v_mul_f32_e32 v4, v67, v63
	v_mfma_f32_32x32x16_bf16 v[16:31], v[94:97], v[76:79], v[16:31]
	v_mul_f32_e32 v0, v67, v56
	v_mul_f32_e32 v1, v67, v57
	v_cvt_pk_bf16_f32 v0, v0, v1
	v_mul_f32_e32 v1, v67, v58
	v_mul_f32_e32 v2, v67, v59
	v_cvt_pk_bf16_f32 v1, v1, v2
	v_mul_f32_e32 v2, v67, v60
	v_mul_f32_e32 v3, v67, v61
	v_cvt_pk_bf16_f32 v2, v2, v3
	v_mul_f32_e32 v3, v67, v62
	v_cvt_pk_bf16_f32 v3, v3, v4
	v_permlane32_swap_b32_e32 v0, v2
	s_nop 0
	v_permlane32_swap_b32_e32 v1, v3
	global_store_dwordx4 v[64:65], v[0:3], off offset:96
	v_mul_f32_e32 v4, v67, v39
	s_lshl_b32 s2, s20, 8
	v_mul_f32_e32 v0, v67, v32
	v_mul_f32_e32 v1, v67, v33
	v_cvt_pk_bf16_f32 v0, v0, v1
	v_mul_f32_e32 v1, v67, v34
	v_mul_f32_e32 v2, v67, v35
	v_cvt_pk_bf16_f32 v1, v1, v2
	v_mul_f32_e32 v2, v67, v36
	v_mul_f32_e32 v3, v67, v37
	v_cvt_pk_bf16_f32 v2, v2, v3
	v_mul_f32_e32 v3, v67, v38
	v_cvt_pk_bf16_f32 v3, v3, v4
	v_permlane32_swap_b32_e32 v0, v2
	s_nop 0
	v_permlane32_swap_b32_e32 v1, v3
	global_store_dwordx4 v[64:65], v[0:3], off offset:128
	v_mul_f32_e32 v4, v67, v47
	s_add_i32 s3, s2, s94
	v_mul_f32_e32 v0, v67, v40
	v_mul_f32_e32 v1, v67, v41
	v_cvt_pk_bf16_f32 v0, v0, v1
	v_mul_f32_e32 v1, v67, v42
	v_mul_f32_e32 v2, v67, v43
	v_cvt_pk_bf16_f32 v1, v1, v2
	v_mul_f32_e32 v2, v67, v44
	v_mul_f32_e32 v3, v67, v45
	v_cvt_pk_bf16_f32 v2, v2, v3
	v_mul_f32_e32 v3, v67, v46
	v_cvt_pk_bf16_f32 v3, v3, v4
	v_permlane32_swap_b32_e32 v0, v2
	s_nop 0
	v_permlane32_swap_b32_e32 v1, v3
	global_store_dwordx4 v[64:65], v[0:3], off offset:160
	v_mul_f32_e32 v4, v67, v23
	s_cmp_lt_i32 s3, s37
	v_mul_f32_e32 v0, v67, v16
	v_mul_f32_e32 v1, v67, v17
	v_cvt_pk_bf16_f32 v0, v0, v1
	v_mul_f32_e32 v1, v67, v18
	v_mul_f32_e32 v2, v67, v19
	v_cvt_pk_bf16_f32 v1, v1, v2
	v_mul_f32_e32 v2, v67, v20
	v_mul_f32_e32 v3, v67, v21
	v_cvt_pk_bf16_f32 v2, v2, v3
	v_mul_f32_e32 v3, v67, v22
	v_cvt_pk_bf16_f32 v3, v3, v4
	v_permlane32_swap_b32_e32 v0, v2
	s_nop 0
	v_permlane32_swap_b32_e32 v1, v3
	global_store_dwordx4 v[64:65], v[0:3], off offset:192
	v_mul_f32_e32 v4, v67, v31
	s_movk_i32 s33, 0xffef
	v_mul_f32_e32 v0, v67, v24
	v_mul_f32_e32 v1, v67, v25
	v_cvt_pk_bf16_f32 v0, v0, v1
	v_mul_f32_e32 v1, v67, v26
	v_mul_f32_e32 v2, v67, v27
	v_cvt_pk_bf16_f32 v1, v1, v2
	v_mul_f32_e32 v2, v67, v28
	v_mul_f32_e32 v3, v67, v29
	v_cvt_pk_bf16_f32 v2, v2, v3
	v_mul_f32_e32 v3, v67, v30
	v_cvt_pk_bf16_f32 v3, v3, v4
	v_permlane32_swap_b32_e32 v0, v2
	s_nop 0
	v_permlane32_swap_b32_e32 v1, v3
	global_store_dwordx4 v[64:65], v[0:3], off offset:224
	s_cbranch_scc0 .LBB0_889

.Lgqa_slow_887:
	ds_read_b128 v[96:99], v216 offset:49152
	ds_read_b128 v[100:103], v216 offset:57344
	v_exp_f32_e32 v80, v80
	v_exp_f32_e32 v81, v81
	v_exp_f32_e32 v88, v88
	s_waitcnt lgkmcnt(1)
	v_mfma_f32_32x32x16_bf16 v[112:127], v[96:99], v[138:141], 0
	v_exp_f32_e32 v89, v89
	v_exp_f32_e32 v82, v82
	v_exp_f32_e32 v90, v90
	v_exp_f32_e32 v83, v83
	v_exp_f32_e32 v91, v91
	v_exp_f32_e32 v84, v84
	v_exp_f32_e32 v92, v92
	s_waitcnt lgkmcnt(0)
	v_mfma_f32_32x32x16_bf16 v[96:111], v[100:103], v[138:141], 0
	ds_read_b128 v[138:141], v218 offset:49152
	s_waitcnt vmcnt(3)
	ds_read_b128 v[162:165], v218 offset:57344
	v_exp_f32_e32 v85, v85
	v_exp_f32_e32 v93, v93
	v_add_f32_e32 v128, v64, v65
	v_exp_f32_e32 v86, v86
	v_exp_f32_e32 v94, v94
	v_add_f32_e32 v128, v66, v128
	s_waitcnt lgkmcnt(1)
	v_mfma_f32_32x32x16_bf16 v[112:127], v[138:141], v[154:157], v[112:127]
	v_exp_f32_e32 v87, v87
	v_exp_f32_e32 v95, v95
	v_add_f32_e32 v128, v67, v128
	v_add_f32_e32 v128, v68, v128
	v_add_f32_e32 v128, v69, v128
	v_add_f32_e32 v128, v70, v128
	v_add_f32_e32 v128, v71, v128
	s_waitcnt lgkmcnt(0)
	v_mfma_f32_32x32x16_bf16 v[96:111], v[162:165], v[154:157], v[96:111]
	ds_read_b128 v[138:141], v219 offset:49152
	ds_read_b128 v[154:157], v219 offset:57344
	s_waitcnt lgkmcnt(1)
	v_mfma_f32_32x32x16_bf16 v[112:127], v[138:141], v[158:161], v[112:127]
	s_waitcnt lgkmcnt(0)
	v_mfma_f32_32x32x16_bf16 v[96:111], v[154:157], v[158:161], v[96:111]
	ds_read_b128 v[138:141], v220 offset:49152
	ds_read_b128 v[154:157], v220 offset:57344
	s_waitcnt lgkmcnt(1)
	v_mfma_f32_32x32x16_bf16 v[112:127], v[138:141], v[150:153], v[112:127]
	s_waitcnt lgkmcnt(0)
	v_mfma_f32_32x32x16_bf16 v[96:111], v[154:157], v[150:153], v[96:111]
	ds_read_b128 v[138:141], v221 offset:49152
	ds_read_b128 v[150:153], v221 offset:57344
	s_waitcnt lgkmcnt(1)
	v_mfma_f32_32x32x16_bf16 v[112:127], v[138:141], v[146:149], v[112:127]
	s_waitcnt lgkmcnt(0)
	v_mfma_f32_32x32x16_bf16 v[96:111], v[150:153], v[146:149], v[96:111]
	ds_read_b128 v[138:141], v222 offset:49152
	ds_read_b128 v[146:149], v222 offset:57344
	s_waitcnt lgkmcnt(1)
	v_mfma_f32_32x32x16_bf16 v[112:127], v[138:141], v[142:145], v[112:127]
	s_waitcnt lgkmcnt(0)
	v_mfma_f32_32x32x16_bf16 v[96:111], v[146:149], v[142:145], v[96:111]
	ds_read_b128 v[138:141], v224 offset:49152
	ds_read_b128 v[142:145], v224 offset:57344
	s_waitcnt lgkmcnt(1)
	v_mfma_f32_32x32x16_bf16 v[112:127], v[138:141], v[134:137], v[112:127]
	s_waitcnt lgkmcnt(0)
	v_mfma_f32_32x32x16_bf16 v[96:111], v[142:145], v[134:137], v[96:111]
	ds_read_b128 v[134:137], v223 offset:49152
	ds_read_b128 v[138:141], v223 offset:57344
	s_waitcnt lgkmcnt(1)
	v_mfma_f32_32x32x16_bf16 v[112:127], v[134:137], v[130:133], v[112:127]
	s_waitcnt lgkmcnt(0)
	v_mfma_f32_32x32x16_bf16 v[96:111], v[138:141], v[130:133], v[96:111]
	v_add_f32_e32 v130, v72, v73
	v_add_f32_e32 v131, v80, v81
	v_add_f32_e32 v132, v88, v89
	v_add_f32_e32 v130, v74, v130
	v_add_f32_e32 v131, v82, v131
	v_add_f32_e32 v132, v90, v132
	v_add_f32_e32 v130, v75, v130
	v_add_f32_e32 v131, v83, v131
	v_add_f32_e32 v132, v91, v132
	v_add_f32_e32 v130, v76, v130
	v_add_f32_e32 v131, v84, v131
	v_add_f32_e32 v132, v92, v132
	v_add_f32_e32 v130, v77, v130
	v_add_f32_e32 v131, v85, v131
	v_add_f32_e32 v132, v93, v132
	v_add_f32_e32 v130, v78, v130
	v_add_f32_e32 v131, v86, v131
	v_add_f32_e32 v132, v94, v132
	v_add_f32_e32 v130, v79, v130
	v_add_f32_e32 v131, v87, v131
	v_add_f32_e32 v132, v95, v132
	v_add_f32_e32 v128, v130, v128
	v_add_f32_e32 v130, v132, v131
	v_add_f32_e32 v142, v128, v130
	v_mov_b32_e32 v143, v142
	v_cvt_pk_bf16_f32 v130, v64, v65
	v_cvt_pk_bf16_f32 v131, v66, v67
	v_cvt_pk_bf16_f32 v132, v68, v69
	v_cvt_pk_bf16_f32 v133, v70, v71
	v_cvt_pk_bf16_f32 v72, v72, v73
	v_cvt_pk_bf16_f32 v73, v74, v75
	v_cvt_pk_bf16_f32 v74, v76, v77
	v_cvt_pk_bf16_f32 v75, v78, v79
	s_nop 1
	v_permlane32_swap_b32_e32 v142, v143
	v_permlane32_swap_b32_e32 v72, v74
	v_permlane32_swap_b32_e32 v73, v75
	v_cvt_pk_bf16_f32 v138, v80, v81
	v_cvt_pk_bf16_f32 v139, v82, v83
	v_cvt_pk_bf16_f32 v140, v84, v85
	v_cvt_pk_bf16_f32 v141, v86, v87
	v_cvt_pk_bf16_f32 v134, v88, v89
	v_cvt_pk_bf16_f32 v135, v90, v91
	v_cvt_pk_bf16_f32 v136, v92, v93
	v_cvt_pk_bf16_f32 v137, v94, v95
	v_permlane32_swap_b32_e32 v130, v132
	v_permlane32_swap_b32_e32 v131, v133
	v_permlane32_swap_b32_e32 v138, v140
	v_permlane32_swap_b32_e32 v139, v141
	v_permlane32_swap_b32_e32 v134, v136
	v_permlane32_swap_b32_e32 v135, v137
	ds_read_b64_tr_b16 v[64:65], v209 offset:0
	ds_read_b64_tr_b16 v[66:67], v209 offset:0x800
	ds_read_b64_tr_b16 v[68:69], v209 offset:0x1000
	ds_read_b64_tr_b16 v[70:71], v209 offset:0x1800
	ds_read_b64_tr_b16 v[76:77], v209 offset:0x2000
	ds_read_b64_tr_b16 v[78:79], v209 offset:0x2800
	ds_read_b64_tr_b16 v[80:81], v209 offset:0x3000
	ds_read_b64_tr_b16 v[82:83], v209 offset:0x3800
	s_waitcnt lgkmcnt(0)
	s_nop 0
	v_mfma_f32_32x32x16_bf16 v[0:15], v[64:67], v[130:133], v[0:15]
	v_max_f32_e32 v64, v97, v97
	v_max_f32_e32 v65, v96, v96
	v_max_f32_e32 v64, v65, v64
	v_max3_f32 v65, v112, v113, v114
	v_max3_f32 v64, v64, v98, v99
	v_max3_f32 v65, v65, v115, v116
	v_max3_f32 v64, v64, v100, v101
	v_mfma_f32_32x32x16_bf16 v[0:15], v[68:71], v[72:75], v[0:15]
	v_max3_f32 v65, v65, v117, v118
	v_max3_f32 v64, v64, v102, v103
	v_max3_f32 v65, v65, v119, v120
	v_max3_f32 v64, v64, v104, v105
	v_max3_f32 v65, v65, v121, v122
	v_max3_f32 v64, v64, v106, v107
	v_max3_f32 v65, v65, v123, v124
	v_mfma_f32_32x32x16_bf16 v[0:15], v[76:79], v[138:141], v[0:15]
	v_max3_f32 v64, v64, v108, v109
	v_max3_f32 v65, v65, v125, v126
	v_max3_f32 v64, v64, v110, v111
	v_max3_f32 v84, v65, v127, v64
	ds_read_b64_tr_b16 v[64:65], v209 offset:0x200
	ds_read_b64_tr_b16 v[66:67], v209 offset:0xa00
	ds_read_b64_tr_b16 v[68:69], v209 offset:0x1200
	v_mfma_f32_32x32x16_bf16 v[0:15], v[80:83], v[134:137], v[0:15]
	ds_read_b64_tr_b16 v[70:71], v209 offset:0x1a00
	ds_read_b64_tr_b16 v[76:77], v209 offset:0x2200
	ds_read_b64_tr_b16 v[78:79], v209 offset:0x2a00
	ds_read_b64_tr_b16 v[80:81], v209 offset:0x3200
	ds_read_b64_tr_b16 v[82:83], v209 offset:0x3a00
	s_waitcnt lgkmcnt(0)
	v_mfma_f32_32x32x16_bf16 v[48:63], v[64:67], v[130:133], v[48:63]
	v_mov_b32_e32 v64, v84
	s_nop 1
	v_permlane32_swap_b32_e32 v84, v64
	v_max_f32_e32 v64, v64, v64
	v_max_f32_e32 v65, v84, v84
	v_max_f32_e32 v64, v65, v64
	v_sub_f32_e32 v65, v64, v226
	v_mfma_f32_32x32x16_bf16 v[48:63], v[68:71], v[72:75], v[48:63]
	v_cmp_ge_f32_e32 vcc, s31, v65
	v_max_f32_e32 v65, v226, v226
	v_max_f32_e32 v64, v65, v64
	v_sub_f32_e32 v65, v226, v64
	v_mul_f32_e32 v65, 0x3e0293ee, v65
	v_exp_f32_e32 v65, v65
	s_cmp_eq_u64 vcc, exec
	v_mfma_f32_32x32x16_bf16 v[48:63], v[76:79], v[138:141], v[48:63]
	s_cselect_b64 vcc, -1, 0
	v_cndmask_b32_e32 v64, v64, v226, vcc
	v_cndmask_b32_e64 v128, v65, 1.0, vcc
	v_mul_f32_e32 v144, 0xbe0293ee, v64
	ds_read_b64_tr_b16 v[64:65], v209 offset:0x400
	ds_read_b64_tr_b16 v[66:67], v209 offset:0xc00
	ds_read_b64_tr_b16 v[68:69], v209 offset:0x1400
	v_mfma_f32_32x32x16_bf16 v[48:63], v[80:83], v[134:137], v[48:63]
	ds_read_b64_tr_b16 v[70:71], v209 offset:0x1c00
	ds_read_b64_tr_b16 v[76:77], v209 offset:0x2400
	ds_read_b64_tr_b16 v[78:79], v209 offset:0x2c00
	ds_read_b64_tr_b16 v[80:81], v209 offset:0x3400
	ds_read_b64_tr_b16 v[82:83], v209 offset:0x3c00
	s_waitcnt lgkmcnt(0)
	v_fmamk_f32 v112, v112, 0x3e0293ee, v144
	v_fmamk_f32 v113, v113, 0x3e0293ee, v144
	v_fmamk_f32 v114, v114, 0x3e0293ee, v144
	v_fmamk_f32 v115, v115, 0x3e0293ee, v144
	v_fmamk_f32 v116, v116, 0x3e0293ee, v144
	v_fmamk_f32 v117, v117, 0x3e0293ee, v144
	v_fmamk_f32 v118, v118, 0x3e0293ee, v144
	v_fmamk_f32 v119, v119, 0x3e0293ee, v144
	v_fmamk_f32 v120, v120, 0x3e0293ee, v144
	v_fmamk_f32 v121, v121, 0x3e0293ee, v144
	v_fmamk_f32 v122, v122, 0x3e0293ee, v144
	v_fmamk_f32 v123, v123, 0x3e0293ee, v144
	v_fmamk_f32 v124, v124, 0x3e0293ee, v144
	v_fmamk_f32 v125, v125, 0x3e0293ee, v144
	v_fmamk_f32 v126, v126, 0x3e0293ee, v144
	v_fmamk_f32 v127, v127, 0x3e0293ee, v144
	v_mfma_f32_32x32x16_bf16 v[32:47], v[64:67], v[130:133], v[32:47]
	v_fma_f32 v84, v100, s52, v144
	v_fma_f32 v85, v101, s52, v144
	v_fma_f32 v86, v102, s52, v144
	v_fma_f32 v87, v103, s52, v144
	v_fma_f32 v88, v104, s52, v144
	v_fma_f32 v89, v105, s52, v144
	v_pk_fma_f32 v[90:91], v[106:107], s[52:53], v[144:145] op_sel_hi:[1,0,0]
	v_exp_f32_e32 v64, v112
	v_exp_f32_e32 v65, v113
	v_exp_f32_e32 v66, v114
	v_mfma_f32_32x32x16_bf16 v[32:47], v[68:71], v[72:75], v[32:47]
	v_exp_f32_e32 v67, v115
	v_exp_f32_e32 v68, v116
	v_exp_f32_e32 v69, v117
	v_exp_f32_e32 v70, v118
	v_exp_f32_e32 v71, v119
	v_pk_fma_f32 v[94:95], v[110:111], s[52:53], v[144:145] op_sel_hi:[1,0,0]
	v_pk_fma_f32 v[92:93], v[108:109], s[52:53], v[144:145] op_sel_hi:[1,0,0]
	v_mfma_f32_32x32x16_bf16 v[32:47], v[76:79], v[138:141], v[32:47]
	ds_read_b64_tr_b16 v[76:77], v209 offset:0x600
	ds_read_b64_tr_b16 v[78:79], v209 offset:0xe00
	v_mfma_f32_32x32x16_bf16 v[32:47], v[80:83], v[134:137], v[32:47]
	v_fma_f32 v80, v96, s52, v144
	v_fma_f32 v81, v97, s52, v144
	ds_read_b64_tr_b16 v[96:97], v209 offset:0x1600
	v_fma_f32 v82, v98, s52, v144
	v_fma_f32 v83, v99, s52, v144
	ds_read_b64_tr_b16 v[98:99], v209 offset:0x1e00
	ds_read_b64_tr_b16 v[100:101], v209 offset:0x2600
	ds_read_b64_tr_b16 v[102:103], v209 offset:0x2e00
	ds_read_b64_tr_b16 v[104:105], v209 offset:0x3600
	ds_read_b64_tr_b16 v[106:107], v209 offset:0x3e00
	s_waitcnt lgkmcnt(0)
	v_mfma_f32_32x32x16_bf16 v[16:31], v[76:79], v[130:133], v[16:31]
	v_exp_f32_e32 v76, v124
	v_exp_f32_e32 v77, v125
	v_exp_f32_e32 v78, v126
	v_exp_f32_e32 v79, v127
	v_cmp_gt_f32_e32 vcc, 1.0, v128
	v_mfma_f32_32x32x16_bf16 v[16:31], v[96:99], v[72:75], v[16:31]
	v_exp_f32_e32 v72, v120
	v_exp_f32_e32 v73, v121
	v_exp_f32_e32 v74, v122
	v_exp_f32_e32 v75, v123
	s_barrier
	v_mfma_f32_32x32x16_bf16 v[16:31], v[100:103], v[138:141], v[16:31]
	v_mfma_f32_32x32x16_bf16 v[16:31], v[104:107], v[134:137], v[16:31]
	s_cbranch_vccz .Lgqa_slow_873
	v_pk_mul_f32 v[14:15], v[14:15], v[128:129] op_sel_hi:[1,0]
	v_pk_mul_f32 v[12:13], v[12:13], v[128:129] op_sel_hi:[1,0]
	v_pk_mul_f32 v[10:11], v[10:11], v[128:129] op_sel_hi:[1,0]
	v_pk_mul_f32 v[8:9], v[8:9], v[128:129] op_sel_hi:[1,0]
	v_pk_mul_f32 v[6:7], v[6:7], v[128:129] op_sel_hi:[1,0]
	v_pk_mul_f32 v[4:5], v[4:5], v[128:129] op_sel_hi:[1,0]
	v_pk_mul_f32 v[2:3], v[2:3], v[128:129] op_sel_hi:[1,0]
	v_pk_mul_f32 v[0:1], v[0:1], v[128:129] op_sel_hi:[1,0]
	v_pk_mul_f32 v[62:63], v[62:63], v[128:129] op_sel_hi:[1,0]
	v_pk_mul_f32 v[60:61], v[60:61], v[128:129] op_sel_hi:[1,0]
	v_pk_mul_f32 v[58:59], v[58:59], v[128:129] op_sel_hi:[1,0]
	v_pk_mul_f32 v[56:57], v[56:57], v[128:129] op_sel_hi:[1,0]
	v_pk_mul_f32 v[54:55], v[54:55], v[128:129] op_sel_hi:[1,0]
	v_pk_mul_f32 v[52:53], v[52:53], v[128:129] op_sel_hi:[1,0]
	v_pk_mul_f32 v[50:51], v[50:51], v[128:129] op_sel_hi:[1,0]
	v_pk_mul_f32 v[48:49], v[48:49], v[128:129] op_sel_hi:[1,0]
	v_pk_mul_f32 v[46:47], v[128:129], v[46:47] op_sel_hi:[0,1]
	v_pk_mul_f32 v[44:45], v[128:129], v[44:45] op_sel_hi:[0,1]
	v_pk_mul_f32 v[42:43], v[128:129], v[42:43] op_sel_hi:[0,1]
	v_pk_mul_f32 v[40:41], v[128:129], v[40:41] op_sel_hi:[0,1]
	v_pk_mul_f32 v[38:39], v[128:129], v[38:39] op_sel_hi:[0,1]
	v_pk_mul_f32 v[36:37], v[128:129], v[36:37] op_sel_hi:[0,1]
	v_pk_mul_f32 v[34:35], v[128:129], v[34:35] op_sel_hi:[0,1]
	v_pk_mul_f32 v[32:33], v[128:129], v[32:33] op_sel_hi:[0,1]
	v_pk_mul_f32 v[30:31], v[128:129], v[30:31] op_sel_hi:[0,1]
	v_pk_mul_f32 v[28:29], v[128:129], v[28:29] op_sel_hi:[0,1]
	v_pk_mul_f32 v[26:27], v[128:129], v[26:27] op_sel_hi:[0,1]
	v_pk_mul_f32 v[24:25], v[128:129], v[24:25] op_sel_hi:[0,1]
	v_pk_mul_f32 v[22:23], v[128:129], v[22:23] op_sel_hi:[0,1]
	v_pk_mul_f32 v[20:21], v[128:129], v[20:21] op_sel_hi:[0,1]
	v_pk_mul_f32 v[18:19], v[128:129], v[18:19] op_sel_hi:[0,1]
	v_pk_mul_f32 v[16:17], v[128:129], v[16:17] op_sel_hi:[0,1]
	s_branch .Lgqa_slow_873
	.section	.rodata,"a",@progbits
	.p2align	6, 0x0
